# s_sleep 1 ahead of the exp block in every softmax section (A and B loops)
# baseline (speedup 1.0000x reference)
; #define ATT_SBAR() __builtin_amdgcn_sched_barrier(0)
; #define ATT_PK4(P, BASE, OUT) do { u32x4 w = {cvtpk(P[BASE + 0], P[BASE + 1]), cvtpk(P[BASE + 2], P[BASE + 3]), cvtpk(P[BASE + 4], P[BASE + 5]), cvtpk(P[BASE + 6], P[BASE + 7])}; \
;     OUT = *reinterpret_cast<bf16x8*>(&w); } while (0)
; #define ATT_WRITE_K(so) do { *(bf16x8*)(K_lds + (so) + kswz<DQK>(kr, kc * 2)) = sk0; if constexpr (DQK == 128) *(bf16x8*)(K_lds + (so) + kswz<DQK>(32 + kr, kc * 2)) = sk1; } while (0)
; #define ATT_WRITE_V(so) do { *(bf16x8*)(V_lds + (so) + vst0) = sv0; *(bf16x8*)(V_lds + (so) + vst1) = sv1; } while (0)
; #define ATT_BAR() do { ATT_SBAR(); asm volatile("s_barrier" ::: "memory"); ATT_SBAR(); } while (0)
; #define ATT_VPAIR(buf, so, blk, ks) do { if constexpr (!(ABL & 8) && !(ABL & 32)) { buf[2 * (ks)] = vtr(vq0 + (so) + v_rd_off(blk, ks, 0)); buf[2 * (ks) + 1] = vtr(vq0 + (so) + v_rd_off(blk, ks, 1)); } } while (0)
; __device__ __forceinline__ void softmax_exp_pack(f32x16& p0, f32x16& p1, bf16x8& pa0, bf16x8& pa1, bf16x8& pa2, bf16x8& pa3) {
;     ...
;   for (int r = 0; r < 16; ++r) { p0[r] = __builtin_amdgcn_exp2f(p0[r]); p1[r] = __builtin_amdgcn_exp2f(p1[r]); }
;     ...
;   ATT_PK4(p0, 0, pa0); ATT_PK4(p0, 8, pa1); ATT_PK4(p1, 0, pa2); ATT_PK4(p1, 8, pa3);
;     ...
;     if constexpr (!(ABL & 4)) { ATT_WRITE_K(k2); ATT_WRITE_V(v1); }
;     ATT_SBAR();
; #pragma unroll
;     for (int ks = 0; ks < 4; ++ks) ATT_VPAIR(va, v0, 0, ks);
;     asm volatile("s_waitcnt lgkmcnt(8)" ::: "memory"); ATT_BAR();
.LBB0_266:
	s_sleep 1
	v_exp_f32_e32 v98, v98
	v_exp_f32_e32 v114, v114
	v_exp_f32_e32 v99, v99
	v_exp_f32_e32 v115, v115
	v_exp_f32_e32 v100, v100
	v_exp_f32_e32 v101, v101
	v_exp_f32_e32 v102, v102
	v_exp_f32_e32 v103, v103
	v_exp_f32_e32 v106, v106
	v_exp_f32_e32 v107, v107
	v_exp_f32_e32 v116, v116
	v_exp_f32_e32 v117, v117
	v_exp_f32_e32 v118, v118
	v_exp_f32_e32 v119, v119
	v_exp_f32_e32 v104, v104
	v_exp_f32_e32 v120, v120
	v_exp_f32_e32 v105, v105
	v_exp_f32_e32 v121, v121
	v_exp_f32_e32 v122, v122
	v_exp_f32_e32 v123, v123
	v_exp_f32_e32 v108, v108
	v_exp_f32_e32 v124, v124
	v_exp_f32_e32 v109, v109
	v_exp_f32_e32 v125, v125
	v_exp_f32_e32 v110, v110
	v_exp_f32_e32 v126, v126
	v_exp_f32_e32 v111, v111
	v_exp_f32_e32 v127, v127
	v_exp_f32_e32 v112, v112
	v_exp_f32_e32 v128, v128
	v_exp_f32_e32 v113, v113
	v_exp_f32_e32 v129, v129
	s_add_i32 s14, s92, 0
	v_cvt_pk_bf16_f32 v98, v98, v99
	v_cvt_pk_bf16_f32 v99, v100, v101
	v_cvt_pk_bf16_f32 v100, v102, v103
	v_cvt_pk_bf16_f32 v102, v106, v107
	v_cvt_pk_bf16_f32 v106, v114, v115
	v_add_u32_e32 v114, s14, v186
	s_add_i32 s14, s93, 0
	s_waitcnt vmcnt(3)
	ds_write_b128 v114, v[224:227] offset:49152
	s_waitcnt vmcnt(2)
	ds_write_b128 v114, v[228:231] offset:57856
	v_add_u32_e32 v114, s14, v189
	v_cvt_pk_bf16_f32 v101, v104, v105
	v_cvt_pk_bf16_f32 v103, v108, v109
	v_cvt_pk_bf16_f32 v104, v110, v111
	v_cvt_pk_bf16_f32 v105, v112, v113
	v_cvt_pk_bf16_f32 v107, v116, v117
	v_cvt_pk_bf16_f32 v108, v118, v119
	v_cvt_pk_bf16_f32 v109, v120, v121
	v_cvt_pk_bf16_f32 v110, v122, v123
	v_cvt_pk_bf16_f32 v111, v124, v125
	v_cvt_pk_bf16_f32 v112, v126, v127
	v_cvt_pk_bf16_f32 v113, v128, v129
	s_waitcnt vmcnt(1)
	ds_write_b128 v114, v[232:235]
	v_add_u32_e32 v114, s14, v190
	s_waitcnt vmcnt(0)
	ds_write_b128 v114, v[236:239]
	v_add_u32_e32 v172, s97, v131
	ds_read_b64_tr_b16 v[114:115], v172
	ds_read_b64_tr_b16 v[116:117], v172 offset:2048
	ds_read_b64_tr_b16 v[118:119], v172 offset:4096
	ds_read_b64_tr_b16 v[120:121], v172 offset:6144
	ds_read_b64_tr_b16 v[122:123], v172 offset:8192
	ds_read_b64_tr_b16 v[124:125], v172 offset:10240
	ds_read_b64_tr_b16 v[126:127], v172 offset:12288
	ds_read_b64_tr_b16 v[128:129], v172 offset:14336
	s_waitcnt lgkmcnt(8)
	s_barrier
; #define ATT_SBAR() __builtin_amdgcn_sched_barrier(0)
; __device__ __forceinline__ unsigned cvtpk(float lo, float hi) { f32x2_t v = {lo, hi}; bf16x2_t b = __builtin_convertvector(v, bf16x2_t); return __builtin_bit_cast(unsigned, b); }
; #define ATT_LOAD_K(t) do { const unsigned so_ = (unsigned)(t) * (unsigned)(KVBLK * LDK * 2); sk0 = __builtin_bit_cast(bf16x8, __builtin_amdgcn_raw_buffer_load_b128(krs, koff, so_, 0)); \
;     if constexpr (DQK == 128) sk1 = __builtin_bit_cast(bf16x8, __builtin_amdgcn_raw_buffer_load_b128(krs, koff, so_ + (unsigned)(32 * LDK * 2), 0)); } while (0)
; #define ATT_LOAD_V(t) do { const unsigned so_ = (unsigned)(t) * (unsigned)(KVBLK * LDV * 2); sv0 = __builtin_bit_cast(bf16x8, __builtin_amdgcn_raw_buffer_load_b128(vrs, voff, so_, 0)); \
;     sv1 = __builtin_bit_cast(bf16x8, __builtin_amdgcn_raw_buffer_load_b128(vrs, voff, so_ + (unsigned)(32 * LDV * 2), 0)); } while (0)
; #define ATT_WRITE_K(so) do { *(bf16x8*)(K_lds + (so) + kswz<DQK>(kr, kc * 2)) = sk0; if constexpr (DQK == 128) *(bf16x8*)(K_lds + (so) + kswz<DQK>(32 + kr, kc * 2)) = sk1; } while (0)
;     ...
;   for (int t = 0; t + 1 < NT; ++t) {
;     if constexpr (ABL & 1) { u32x4 w0 = {cvtpk(p0[0], p0[1]), cvtpk(p0[2], p0[3]), cvtpk(p0[4], p0[5]), cvtpk(p0[6], p0[7])}, w1 = {cvtpk(p0[8], p0[9]), cvtpk(p0[10], p0[11]), cvtpk(p0[12], p0[13]), cvtpk(p0[14], p0[15])};
;         u32x4 w2 = {cvtpk(p1[0], p1[1]), cvtpk(p1[2], p1[3]), cvtpk(p1[4], p1[5]), cvtpk(p1[6], p1[7])}, w3 = {cvtpk(p1[8], p1[9]), cvtpk(p1[10], p1[11]), cvtpk(p1[12], p1[13]), cvtpk(p1[14], p1[15])};
;         pa0 = *reinterpret_cast<bf16x8*>(&w0); pa1 = *reinterpret_cast<bf16x8*>(&w1); pa2 = *reinterpret_cast<bf16x8*>(&w2); pa3 = *reinterpret_cast<bf16x8*>(&w3); }
;     else { ATT_SOFTMAX(t == 0); }
;     if constexpr (!(ABL & 4)) { ATT_WRITE_K(k2); ATT_WRITE_V(v1); }
;     ATT_SBAR();
; #pragma unroll
;     for (int ks = 0; ks < 4; ++ks) ATT_VPAIR(va, v0, 0, ks);
;     asm volatile("s_waitcnt lgkmcnt(8)" ::: "memory"); ATT_BAR();
;     ATT_XSECTION(true);
;     if constexpr (!(ABL & 4)) { const int tk = (t + 3 < NT) ? t + 3 : NT - 1, tv = (t + 2 < NT) ? t + 2 : NT - 1; ATT_LOAD_K(tk); ATT_LOAD_V(tv); }
;     ATT_BAR();
;     { const int tk_ = k0; k0 = k1; k1 = k2; k2 = tk_; const int tv_ = v0; v0 = v1; v1 = v2; v2 = tv_; }
	s_setprio 2
	s_waitcnt lgkmcnt(6)
	v_mfma_f32_32x32x16_bf16 v[18:33], v[98:101], v[114:117], v[18:33]
	ds_read_b64_tr_b16 v[168:169], v172 offset:512
	ds_read_b64_tr_b16 v[170:171], v172 offset:2560
	s_waitcnt lgkmcnt(6)
	v_mfma_f32_32x32x16_bf16 v[18:33], v[102:105], v[118:121], v[18:33]
	ds_read_b64_tr_b16 v[114:115], v172 offset:4608
	ds_read_b64_tr_b16 v[116:117], v172 offset:6656
	s_waitcnt lgkmcnt(6)
	v_mfma_f32_32x32x16_bf16 v[18:33], v[106:109], v[122:125], v[18:33]
	ds_read_b64_tr_b16 v[118:119], v172 offset:8704
	ds_read_b64_tr_b16 v[120:121], v172 offset:10752
	s_waitcnt lgkmcnt(6)
	v_mfma_f32_32x32x16_bf16 v[18:33], v[110:113], v[126:129], v[18:33]
	ds_read_b64_tr_b16 v[122:123], v172 offset:12800
	ds_read_b64_tr_b16 v[124:125], v172 offset:14848
	s_waitcnt lgkmcnt(6)
	v_mfma_f32_32x32x16_bf16 v[34:49], v[98:101], v[168:171], v[34:49]
	ds_read_b64_tr_b16 v[126:127], v172 offset:1024
	ds_read_b64_tr_b16 v[128:129], v172 offset:3072
	s_waitcnt lgkmcnt(6)
	v_mfma_f32_32x32x16_bf16 v[34:49], v[102:105], v[114:117], v[34:49]
	ds_read_b64_tr_b16 v[168:169], v172 offset:5120
	ds_read_b64_tr_b16 v[170:171], v172 offset:7168
	s_waitcnt lgkmcnt(6)
	v_mfma_f32_32x32x16_bf16 v[34:49], v[106:109], v[118:121], v[34:49]
	ds_read_b64_tr_b16 v[114:115], v172 offset:9216
	ds_read_b64_tr_b16 v[116:117], v172 offset:11264
	s_waitcnt lgkmcnt(6)
	v_mfma_f32_32x32x16_bf16 v[34:49], v[110:113], v[122:125], v[34:49]
	ds_read_b64_tr_b16 v[118:119], v172 offset:13312
	ds_read_b64_tr_b16 v[120:121], v172 offset:15360
	s_waitcnt lgkmcnt(6)
	v_mfma_f32_32x32x16_bf16 v[50:65], v[98:101], v[126:129], v[50:65]
	ds_read_b64_tr_b16 v[122:123], v172 offset:1536
	ds_read_b64_tr_b16 v[124:125], v172 offset:3584
	s_waitcnt lgkmcnt(6)
	v_mfma_f32_32x32x16_bf16 v[50:65], v[102:105], v[168:171], v[50:65]
	ds_read_b64_tr_b16 v[126:127], v172 offset:5632
	ds_read_b64_tr_b16 v[128:129], v172 offset:7680
	s_waitcnt lgkmcnt(6)
	v_mfma_f32_32x32x16_bf16 v[50:65], v[106:109], v[114:117], v[50:65]
	ds_read_b64_tr_b16 v[168:169], v172 offset:9728
	ds_read_b64_tr_b16 v[170:171], v172 offset:11776
	s_waitcnt lgkmcnt(6)
	v_mfma_f32_32x32x16_bf16 v[50:65], v[110:113], v[118:121], v[50:65]
	ds_read_b64_tr_b16 v[114:115], v172 offset:13824
	ds_read_b64_tr_b16 v[116:117], v172 offset:15872
	s_waitcnt lgkmcnt(6)
	v_mfma_f32_32x32x16_bf16 v[66:81], v[98:101], v[122:125], v[66:81]
	v_add_u32_e32 v193, s36, v192
	ds_read_b128 v[118:121], v193 offset:49152
	s_waitcnt lgkmcnt(5)
	v_mfma_f32_32x32x16_bf16 v[66:81], v[102:105], v[126:129], v[66:81]
	ds_read_b128 v[172:175], v193 offset:57856
	s_waitcnt lgkmcnt(4)
	v_mfma_f32_32x32x16_bf16 v[66:81], v[106:109], v[168:171], v[66:81]
	ds_read_b128 v[176:179], v193 offset:49184
	s_waitcnt lgkmcnt(3)
	v_mfma_f32_32x32x16_bf16 v[66:81], v[110:113], v[114:117], v[66:81]
	ds_read_b128 v[168:171], v193 offset:57888
	v_mfma_f32_4x4x4_16b_bf16 v[240:243], v[98:99], v[132:133], v[240:243]
	ds_read_b128 v[180:183], v193 offset:49216
	v_mfma_f32_4x4x4_16b_bf16 v[244:247], v[100:101], v[132:133], v[244:247]
	v_mfma_f32_4x4x4_16b_bf16 v[240:243], v[102:103], v[132:133], v[240:243]
	ds_read_b128 v[194:197], v193 offset:57920
	v_mfma_f32_4x4x4_16b_bf16 v[244:247], v[104:105], v[132:133], v[244:247]
	v_mfma_f32_4x4x4_16b_bf16 v[240:243], v[106:107], v[132:133], v[240:243]
	ds_read_b128 v[198:201], v193 offset:49248
	v_mfma_f32_4x4x4_16b_bf16 v[244:247], v[108:109], v[132:133], v[244:247]
	v_mfma_f32_4x4x4_16b_bf16 v[240:243], v[110:111], v[132:133], v[240:243]
	ds_read_b128 v[212:215], v193 offset:57952
	v_mfma_f32_4x4x4_16b_bf16 v[244:247], v[112:113], v[132:133], v[244:247]
	s_waitcnt lgkmcnt(7)
	v_mfma_f32_32x32x16_bf16 v[98:113], v[118:121], v[136:139], v[82:97]
	ds_read_b128 v[216:219], v193 offset:49280
	s_waitcnt lgkmcnt(7)
	v_mfma_f32_32x32x16_bf16 v[114:129], v[172:175], v[136:139], v[82:97]
	ds_read_b128 v[220:223], v193 offset:57984
	s_waitcnt lgkmcnt(7)
	v_mfma_f32_32x32x16_bf16 v[98:113], v[176:179], v[140:143], v[98:113]
	ds_read_b128 v[172:175], v193 offset:49312
	s_waitcnt lgkmcnt(7)
	v_mfma_f32_32x32x16_bf16 v[114:129], v[168:171], v[140:143], v[114:129]
	ds_read_b128 v[176:179], v193 offset:58016
	s_waitcnt lgkmcnt(7)
	v_mfma_f32_32x32x16_bf16 v[98:113], v[180:183], v[144:147], v[98:113]
	ds_read_b128 v[168:171], v193 offset:49344
	s_waitcnt lgkmcnt(7)
	v_mfma_f32_32x32x16_bf16 v[114:129], v[194:197], v[144:147], v[114:129]
	ds_read_b128 v[180:183], v193 offset:58048
	s_waitcnt lgkmcnt(7)
	v_mfma_f32_32x32x16_bf16 v[98:113], v[198:201], v[148:151], v[98:113]
	ds_read_b128 v[194:197], v193 offset:49376
	s_waitcnt lgkmcnt(7)
	v_mfma_f32_32x32x16_bf16 v[114:129], v[212:215], v[148:151], v[114:129]
	ds_read_b128 v[198:201], v193 offset:58080
	s_waitcnt lgkmcnt(7)
	v_mfma_f32_32x32x16_bf16 v[98:113], v[216:219], v[152:155], v[98:113]
	s_min_u32 s14, s95, 0x7c
	s_lshl_b32 s14, s14, 15
	s_add_i32 s15, s14, 0x18000
	s_add_i32 s14, s14, 0x1c000
	buffer_load_dwordx4 v[224:227], v191, s[8:11], s15 offen
	s_waitcnt lgkmcnt(6)
	v_mfma_f32_32x32x16_bf16 v[114:129], v[220:223], v[152:155], v[114:129]
	buffer_load_dwordx4 v[228:231], v191, s[8:11], s14 offen
	s_waitcnt lgkmcnt(5)
	v_mfma_f32_32x32x16_bf16 v[98:113], v[172:175], v[156:159], v[98:113]
	s_add_i32 s18, s96, 0xffffc000
	s_mov_b32 s14, s10
	s_mov_b32 s15, s11
	buffer_load_dwordx4 v[232:235], v191, s[12:15], s18 offen
	s_waitcnt lgkmcnt(4)
	v_mfma_f32_32x32x16_bf16 v[114:129], v[176:179], v[156:159], v[114:129]
	buffer_load_dwordx4 v[236:239], v191, s[12:15], s96 offen
	s_waitcnt lgkmcnt(3)
	v_mfma_f32_32x32x16_bf16 v[98:113], v[168:171], v[160:163], v[98:113]
	s_waitcnt lgkmcnt(2)
	v_mfma_f32_32x32x16_bf16 v[114:129], v[180:183], v[160:163], v[114:129]
	s_waitcnt lgkmcnt(1)
	v_mfma_f32_32x32x16_bf16 v[98:113], v[194:197], v[164:167], v[98:113]
	s_waitcnt lgkmcnt(0)
	v_mfma_f32_32x32x16_bf16 v[114:129], v[198:201], v[164:167], v[114:129]
	s_setprio 0
	s_barrier
	s_add_i32 s96, s96, 0x8000
	s_add_i32 s95, s95, 1
	s_cmpk_eq_i32 s95, 0x7e
	s_cbranch_scc1 .LBB0_274
	s_mov_b32 s14, s92
	s_mov_b32 s92, s94
	s_mov_b32 s94, s36
	s_mov_b32 s15, s93
	s_mov_b32 s93, s91
	s_mov_b32 s91, s97
	s_branch .LBB0_265
